# P6 LN1 fp8 row stores widened: 8 dword stores per token -> 2 dwordx4 stores via DPP quad transpose, vmcnt counts adjusted
# speedup vs baseline: 1.0058x; 1.0058x over previous
.LBB0_704:
	s_or_b64 exec, exec, s[12:13]
	v_mbcnt_lo_u32_b32 v178, -1, 0
	v_mbcnt_hi_u32_b32 v178, -1, v178
	v_and_b32_e32 v178, 3, v178
	v_mul_u32_u24_e32 v178, 0xfc, v178
	v_mov_b32_e32 v179, 0
	s_mov_b32 s36, -2
	v_mov_b64_e32 v[2:3], v[46:47]
	v_mov_b64_e32 v[4:5], v[44:45]
	s_mov_b32 s37, s40
	s_mov_b64 s[14:15], s[20:21]
	ds_read_b128 v[180:183], v132
	ds_read_b128 v[184:187], v132 offset:8192
	ds_read_b128 v[188:191], v132 offset:1024
	ds_read_b128 v[192:195], v132 offset:9216
	ds_read_b128 v[196:199], v132 offset:2048
	ds_read_b128 v[200:203], v132 offset:10240
	ds_read_b128 v[204:207], v132 offset:3072
	ds_read_b128 v[208:211], v132 offset:11264
	ds_read_b128 v[212:215], v132 offset:4096
	ds_read_b128 v[216:219], v132 offset:12288
	ds_read_b128 v[220:223], v132 offset:5120
	ds_read_b128 v[224:227], v132 offset:13312
	ds_read_b128 v[228:231], v132 offset:6144
	ds_read_b128 v[232:235], v132 offset:14336
	ds_read_b128 v[236:239], v132 offset:7168
	ds_read_b128 v[240:243], v132 offset:15360
	v_lshl_add_u64 v[176:177], s[92:93], 0, v[4:5]
	s_mov_b32 s12, 0x69400000
	s_mov_b32 s13, 0
	v_lshl_add_u64 v[176:177], v[176:177], 0, s[12:13]
	global_load_dwordx2 v[160:161], v[176:177], off
	global_load_dwordx2 v[162:163], v[176:177], off offset:512
	global_load_dwordx2 v[164:165], v[176:177], off offset:1024
	global_load_dwordx2 v[166:167], v[176:177], off offset:1536
	global_load_dwordx2 v[168:169], v[176:177], off offset:2048
	global_load_dwordx2 v[170:171], v[176:177], off offset:2560
	global_load_dwordx2 v[172:173], v[176:177], off offset:3072
	global_load_dwordx2 v[174:175], v[176:177], off offset:3584
	s_waitcnt vmcnt(0)
	s_waitcnt lgkmcnt(0)
	s_branch .LBB0_706

.LBB0_706:
	v_lshl_add_u64 v[8:9], s[92:93], 0, v[4:5]
	v_add_co_u32_e32 v10, vcc, 0x69400000, v8
	v_mov_b32_e32 v144, 0
	s_nop 0
	v_addc_co_u32_e32 v11, vcc, 0, v9, vcc
	v_add_co_u32_e32 v8, vcc, s43, v8
	v_lshl_add_u32 v144, v144, 2, v132
	s_nop 0
	v_addc_co_u32_e32 v9, vcc, 0, v9, vcc
	s_waitcnt vmcnt(4)
	v_lshlrev_b32_e32 v6, 16, v160
	v_and_b32_e32 v7, 0xffff0000, v160
	v_lshlrev_b32_e32 v70, 16, v161
	v_and_b32_e32 v71, 0xffff0000, v161
	v_add_f32_e32 v12, v6, v7
	v_add_f32_e32 v13, v70, v71
	v_add_f32_e32 v12, v12, v13
	v_add_f32_e32 v14, 0, v12
	v_lshlrev_b32_e32 v66, 16, v162
	v_and_b32_e32 v67, 0xffff0000, v162
	v_lshlrev_b32_e32 v68, 16, v163
	v_and_b32_e32 v69, 0xffff0000, v163
	v_add_f32_e32 v12, v66, v67
	v_add_f32_e32 v13, v68, v69
	v_add_f32_e32 v12, v12, v13
	v_add_f32_e32 v14, v14, v12
	v_lshlrev_b32_e32 v64, 16, v164
	v_and_b32_e32 v65, 0xffff0000, v164
	v_lshlrev_b32_e32 v62, 16, v165
	v_and_b32_e32 v63, 0xffff0000, v165
	v_add_f32_e32 v12, v64, v65
	v_add_f32_e32 v13, v62, v63
	v_add_f32_e32 v12, v12, v13
	v_add_f32_e32 v14, v14, v12
	v_lshlrev_b32_e32 v58, 16, v166
	v_and_b32_e32 v59, 0xffff0000, v166
	v_lshlrev_b32_e32 v60, 16, v167
	v_and_b32_e32 v61, 0xffff0000, v167
	v_add_f32_e32 v12, v58, v59
	v_add_f32_e32 v13, v60, v61
	v_add_f32_e32 v12, v12, v13
	v_add_f32_e32 v14, v14, v12
	v_lshlrev_b32_e32 v56, 16, v168
	v_and_b32_e32 v57, 0xffff0000, v168
	v_lshlrev_b32_e32 v54, 16, v169
	v_and_b32_e32 v55, 0xffff0000, v169
	v_add_f32_e32 v12, v56, v57
	v_add_f32_e32 v13, v54, v55
	v_add_f32_e32 v12, v12, v13
	v_add_f32_e32 v14, v14, v12
	v_lshlrev_b32_e32 v32, 16, v170
	v_and_b32_e32 v33, 0xffff0000, v170
	v_lshlrev_b32_e32 v52, 16, v171
	v_and_b32_e32 v53, 0xffff0000, v171
	v_add_f32_e32 v12, v32, v33
	v_add_f32_e32 v13, v52, v53
	v_add_f32_e32 v12, v12, v13
	v_add_f32_e32 v14, v14, v12
	v_lshlrev_b32_e32 v30, 16, v172
	v_and_b32_e32 v31, 0xffff0000, v172
	v_lshlrev_b32_e32 v28, 16, v173
	v_and_b32_e32 v29, 0xffff0000, v173
	v_add_f32_e32 v12, v30, v31
	v_add_f32_e32 v13, v28, v29
	v_add_f32_e32 v12, v12, v13
	v_add_f32_e32 v12, v14, v12
	v_lshlrev_b32_e32 v24, 16, v174
	v_and_b32_e32 v25, 0xffff0000, v174
	v_lshlrev_b32_e32 v26, 16, v175
	v_and_b32_e32 v27, 0xffff0000, v175
	v_add_f32_e32 v10, v24, v25
	v_add_f32_e32 v11, v26, v27
	v_add_f32_e32 v10, v10, v11
	v_add_f32_e32 v34, v12, v10
	global_load_dwordx2 v[22:23], v[8:9], off
	global_load_dwordx2 v[20:21], v[8:9], off offset:512
	global_load_dwordx2 v[18:19], v[8:9], off offset:1024
	global_load_dwordx2 v[16:17], v[8:9], off offset:1536
	global_load_dwordx2 v[14:15], v[8:9], off offset:2048
	global_load_dwordx2 v[12:13], v[8:9], off offset:2560
	global_load_dwordx2 v[10:11], v[8:9], off offset:3072
	s_nop 0
	global_load_dwordx2 v[8:9], v[8:9], off offset:3584
	s_cmp_lt_i32 s36, 4
	s_cselect_b32 s12, s30, 0
	s_cselect_b32 s13, s31, 0
	v_lshl_add_u64 v[176:177], v[4:5], 0, s[12:13]
	v_lshl_add_u64 v[176:177], s[92:93], 0, v[176:177]
	s_mov_b32 s12, 0x69400000
	s_mov_b32 s13, 0
	v_lshl_add_u64 v[176:177], v[176:177], 0, s[12:13]
	global_load_dwordx2 v[160:161], v[176:177], off
	global_load_dwordx2 v[162:163], v[176:177], off offset:512
	global_load_dwordx2 v[164:165], v[176:177], off offset:1024
	global_load_dwordx2 v[166:167], v[176:177], off offset:1536
	global_load_dwordx2 v[168:169], v[176:177], off offset:2048
	global_load_dwordx2 v[170:171], v[176:177], off offset:2560
	global_load_dwordx2 v[172:173], v[176:177], off offset:3072
	global_load_dwordx2 v[174:175], v[176:177], off offset:3584
	v_add_f32_dpp v34, v34, v34 quad_perm:[1,0,3,2] row_mask:0xf bank_mask:0xf bound_ctrl:1
	s_nop 1
	v_add_f32_dpp v34, v34, v34 quad_perm:[2,3,0,1] row_mask:0xf bank_mask:0xf bound_ctrl:1
	s_nop 1
	v_add_f32_dpp v34, v34, v34 row_half_mirror row_mask:0xf bank_mask:0xf bound_ctrl:1
	s_nop 1
	v_add_f32_dpp v34, v34, v34 row_mirror row_mask:0xf bank_mask:0xf bound_ctrl:1
	v_mov_b32_e32 v145, v34
	s_nop 1
	v_permlane16_swap_b32_e32 v34, v145
	v_add_f32_e32 v34, v34, v145
	v_mov_b32_e32 v145, v34
	s_nop 1
	v_permlane32_swap_b32_e32 v34, v145
	v_add_f32_e32 v145, v34, v145
	v_fmac_f32_e32 v71, 0xba000000, v145
	v_fmac_f32_e32 v7, 0xba000000, v145
	v_fmac_f32_e32 v70, 0xba000000, v145
	v_fmac_f32_e32 v6, 0xba000000, v145
	v_mul_f32_e32 v34, v7, v7
	v_mul_f32_e32 v146, v71, v71
	v_fmac_f32_e32 v34, v6, v6
	v_fmac_f32_e32 v146, v70, v70
	v_fmac_f32_e32 v69, 0xba000000, v145
	v_fmac_f32_e32 v67, 0xba000000, v145
	v_add_f32_e32 v34, v34, v146
	v_fmac_f32_e32 v68, 0xba000000, v145
	v_fmac_f32_e32 v66, 0xba000000, v145
	v_mul_f32_e32 v146, v67, v67
	v_mul_f32_e32 v147, v69, v69
	v_fmac_f32_e32 v146, v66, v66
	v_fmac_f32_e32 v147, v68, v68
	v_add_f32_e32 v146, v146, v147
	v_fmac_f32_e32 v63, 0xba000000, v145
	v_fmac_f32_e32 v65, 0xba000000, v145
	v_add_f32_e32 v34, v34, v146
	v_fmac_f32_e32 v62, 0xba000000, v145
	v_fmac_f32_e32 v64, 0xba000000, v145
	v_mul_f32_e32 v146, v65, v65
	v_mul_f32_e32 v147, v63, v63
	v_fmac_f32_e32 v146, v64, v64
	v_fmac_f32_e32 v147, v62, v62
	v_add_f32_e32 v146, v146, v147
	v_fmac_f32_e32 v61, 0xba000000, v145
	v_fmac_f32_e32 v59, 0xba000000, v145
	v_add_f32_e32 v34, v146, v34
	v_fmac_f32_e32 v60, 0xba000000, v145
	v_fmac_f32_e32 v58, 0xba000000, v145
	v_mul_f32_e32 v146, v59, v59
	v_mul_f32_e32 v147, v61, v61
	v_fmac_f32_e32 v146, v58, v58
	v_fmac_f32_e32 v147, v60, v60
	v_add_f32_e32 v146, v146, v147
	v_fmac_f32_e32 v55, 0xba000000, v145
	v_fmac_f32_e32 v57, 0xba000000, v145
	v_add_f32_e32 v34, v146, v34
	v_fmac_f32_e32 v54, 0xba000000, v145
	v_fmac_f32_e32 v56, 0xba000000, v145
	v_mul_f32_e32 v146, v57, v57
	v_mul_f32_e32 v147, v55, v55
	v_fmac_f32_e32 v146, v56, v56
	v_fmac_f32_e32 v147, v54, v54
	v_add_f32_e32 v146, v146, v147
	v_fmac_f32_e32 v53, 0xba000000, v145
	v_fmac_f32_e32 v33, 0xba000000, v145
	v_add_f32_e32 v34, v146, v34
	v_fmac_f32_e32 v52, 0xba000000, v145
	v_fmac_f32_e32 v32, 0xba000000, v145
	v_mul_f32_e32 v146, v33, v33
	v_mul_f32_e32 v147, v53, v53
	v_fmac_f32_e32 v146, v32, v32
	v_fmac_f32_e32 v147, v52, v52
	v_add_f32_e32 v146, v146, v147
	v_fmac_f32_e32 v29, 0xba000000, v145
	v_fmac_f32_e32 v31, 0xba000000, v145
	v_add_f32_e32 v34, v146, v34
	v_fmac_f32_e32 v28, 0xba000000, v145
	v_fmac_f32_e32 v30, 0xba000000, v145
	v_mul_f32_e32 v146, v31, v31
	v_mul_f32_e32 v147, v29, v29
	v_fmac_f32_e32 v146, v30, v30
	v_fmac_f32_e32 v147, v28, v28
	v_add_f32_e32 v146, v146, v147
	v_fmac_f32_e32 v27, 0xba000000, v145
	v_fmac_f32_e32 v25, 0xba000000, v145
	v_add_f32_e32 v34, v146, v34
	v_fmac_f32_e32 v26, 0xba000000, v145
	v_fmac_f32_e32 v24, 0xba000000, v145
	v_mul_f32_e32 v146, v25, v25
	v_mul_f32_e32 v147, v27, v27
	v_fmac_f32_e32 v146, v24, v24
	v_fmac_f32_e32 v147, v26, v26
	v_add_f32_e32 v146, v146, v147
	v_add_f32_e32 v34, v146, v34
	s_nop 1
	v_add_f32_dpp v34, v34, v34 quad_perm:[1,0,3,2] row_mask:0xf bank_mask:0xf bound_ctrl:1
	s_nop 1
	v_add_f32_dpp v34, v34, v34 quad_perm:[2,3,0,1] row_mask:0xf bank_mask:0xf bound_ctrl:1
	s_nop 1
	v_add_f32_dpp v34, v34, v34 row_half_mirror row_mask:0xf bank_mask:0xf bound_ctrl:1
	s_nop 1
	v_add_f32_dpp v34, v34, v34 row_mirror row_mask:0xf bank_mask:0xf bound_ctrl:1
	v_mov_b32_e32 v146, v34
	s_nop 1
	v_permlane16_swap_b32_e32 v34, v146
	v_add_f32_e32 v34, v34, v146
	v_mov_b32_e32 v146, v34
	s_nop 1
	v_permlane32_swap_b32_e32 v34, v146
	v_add_f32_e32 v34, v34, v146
	v_fmamk_f32 v34, v34, 0x3a000000, v135
	v_cmp_gt_f32_e32 vcc, s44, v34
	v_mul_f32_e32 v146, 0x4f800000, v34
	s_nop 0
	v_cndmask_b32_e32 v34, v34, v146, vcc
	v_sqrt_f32_e32 v146, v34
	s_nop 0
	v_add_u32_e32 v147, -1, v146
	v_fma_f32 v148, -v147, v146, v34
	v_cmp_ge_f32_e64 s[12:13], 0, v148
	v_add_u32_e32 v148, 1, v146
	s_nop 0
	v_cndmask_b32_e64 v147, v146, v147, s[12:13]
	v_fma_f32 v146, -v148, v146, v34
	v_cmp_lt_f32_e64 s[12:13], 0, v146
	s_nop 1
	v_cndmask_b32_e64 v146, v147, v148, s[12:13]
	v_mul_f32_e32 v147, 0x37800000, v146
	v_cndmask_b32_e32 v146, v146, v147, vcc
	v_cmp_class_f32_e32 vcc, v34, v136
	s_nop 1
	v_cndmask_b32_e32 v34, v146, v34, vcc
	v_div_scale_f32 v146, s[12:13], v34, v34, 1.0
	v_rcp_f32_e32 v147, v146
	s_nop 0
	v_fma_f32 v148, -v146, v147, 1.0
	v_fmac_f32_e32 v147, v148, v147
	v_div_scale_f32 v148, vcc, 1.0, v34, 1.0
	v_mul_f32_e32 v149, v148, v147
	v_fma_f32 v150, -v146, v149, v148
	v_fmac_f32_e32 v149, v150, v147
	v_fma_f32 v146, -v146, v149, v148
	v_div_fmas_f32 v146, v146, v147, v149
	v_div_fixup_f32 v34, v146, v34, 1.0
	v_pk_mul_f32 v[6:7], v[6:7], v[34:35] op_sel_hi:[1,0]
	v_pk_mul_f32 v[70:71], v[70:71], v[34:35] op_sel_hi:[1,0]
	v_pk_mul_f32 v[66:67], v[66:67], v[34:35] op_sel_hi:[1,0]
	v_pk_mul_f32 v[68:69], v[68:69], v[34:35] op_sel_hi:[1,0]
	v_pk_fma_f32 v[6:7], v[180:181], v[6:7], v[184:185]
	v_cvt_pk_fp8_f32 v244, v6, v7
	v_pk_fma_f32 v[70:71], v[182:183], v[70:71], v[186:187]
	v_lshl_add_u64 v[6:7], s[92:93], 0, v[2:3]
	v_lshl_add_u64 v[6:7], v[6:7], 0, v[178:179]
	v_pk_mul_f32 v[64:65], v[64:65], v[34:35] op_sel_hi:[1,0]
	v_cvt_pk_fp8_f32 v244, v70, v71 op_sel:[0,0,1]
	v_pk_mul_f32 v[62:63], v[62:63], v[34:35] op_sel_hi:[1,0]
	v_pk_mul_f32 v[58:59], v[58:59], v[34:35] op_sel_hi:[1,0]
	v_pk_mul_f32 v[60:61], v[60:61], v[34:35] op_sel_hi:[1,0]
	v_pk_mul_f32 v[56:57], v[56:57], v[34:35] op_sel_hi:[1,0]
	v_pk_mul_f32 v[54:55], v[54:55], v[34:35] op_sel_hi:[1,0]
	v_pk_mul_f32 v[32:33], v[32:33], v[34:35] op_sel_hi:[1,0]
	v_pk_fma_f32 v[66:67], v[188:189], v[66:67], v[192:193]
	v_pk_fma_f32 v[68:69], v[190:191], v[68:69], v[194:195]
	v_cvt_pk_fp8_f32 v245, v66, v67
	v_pk_mul_f32 v[52:53], v[52:53], v[34:35] op_sel_hi:[1,0]
	v_pk_mul_f32 v[30:31], v[30:31], v[34:35] op_sel_hi:[1,0]
	v_pk_mul_f32 v[28:29], v[28:29], v[34:35] op_sel_hi:[1,0]
	v_cvt_pk_fp8_f32 v245, v68, v69 op_sel:[0,0,1]
	v_pk_mul_f32 v[24:25], v[24:25], v[34:35] op_sel_hi:[1,0]
	v_pk_mul_f32 v[26:27], v[26:27], v[34:35] op_sel_hi:[1,0]
	v_pk_fma_f32 v[64:65], v[64:65], v[196:197], v[200:201]
	v_cvt_pk_fp8_f32 v246, v64, v65
	v_pk_fma_f32 v[62:63], v[62:63], v[198:199], v[202:203]
	s_nop 0
	v_cvt_pk_fp8_f32 v246, v62, v63 op_sel:[0,0,1]
	v_pk_fma_f32 v[58:59], v[58:59], v[204:205], v[208:209]
	v_cvt_pk_fp8_f32 v247, v58, v59
	v_pk_fma_f32 v[60:61], v[60:61], v[206:207], v[210:211]
	s_nop 0
	v_cvt_pk_fp8_f32 v247, v60, v61 op_sel:[0,0,1]
	s_nop 1
	s_mov_b32 vcc_lo, 0x55555555
	s_mov_b32 vcc_hi, 0x55555555
	v_cndmask_b32_dpp v252, v245, v244, vcc quad_perm:[1,0,3,2] row_mask:0xf bank_mask:0xf
	v_cndmask_b32_dpp v253, v247, v246, vcc quad_perm:[1,0,3,2] row_mask:0xf bank_mask:0xf
	s_mov_b32 vcc_lo, 0xaaaaaaaa
	s_mov_b32 vcc_hi, 0xaaaaaaaa
	v_cndmask_b32_dpp v245, v244, v245, vcc quad_perm:[1,0,3,2] row_mask:0xf bank_mask:0xf
	v_cndmask_b32_dpp v247, v246, v247, vcc quad_perm:[1,0,3,2] row_mask:0xf bank_mask:0xf
	s_mov_b32 vcc_lo, 0x33333333
	s_mov_b32 vcc_hi, 0x33333333
	v_cndmask_b32_dpp v248, v253, v252, vcc quad_perm:[2,3,0,1] row_mask:0xf bank_mask:0xf
	v_cndmask_b32_dpp v249, v247, v245, vcc quad_perm:[2,3,0,1] row_mask:0xf bank_mask:0xf
	s_mov_b32 vcc_lo, 0xcccccccc
	s_mov_b32 vcc_hi, 0xcccccccc
	v_cndmask_b32_dpp v250, v252, v253, vcc quad_perm:[2,3,0,1] row_mask:0xf bank_mask:0xf
	v_cndmask_b32_dpp v251, v245, v247, vcc quad_perm:[2,3,0,1] row_mask:0xf bank_mask:0xf
	global_store_dwordx4 v[6:7], v[248:251], off offset:-2048
	v_pk_fma_f32 v[56:57], v[56:57], v[212:213], v[216:217]
	v_cvt_pk_fp8_f32 v244, v56, v57
	v_pk_fma_f32 v[54:55], v[54:55], v[214:215], v[218:219]
	s_nop 0
	v_cvt_pk_fp8_f32 v244, v54, v55 op_sel:[0,0,1]
	v_pk_fma_f32 v[32:33], v[32:33], v[220:221], v[224:225]
	v_cvt_pk_fp8_f32 v245, v32, v33
	v_pk_fma_f32 v[52:53], v[52:53], v[222:223], v[226:227]
	v_cvt_pk_fp8_f32 v245, v52, v53 op_sel:[0,0,1]
	v_pk_fma_f32 v[30:31], v[30:31], v[228:229], v[232:233]
	s_nop 0
	v_cvt_pk_fp8_f32 v246, v30, v31
	v_pk_fma_f32 v[28:29], v[28:29], v[230:231], v[234:235]
	s_nop 0
	v_cvt_pk_fp8_f32 v246, v28, v29 op_sel:[0,0,1]
	v_pk_fma_f32 v[24:25], v[24:25], v[236:237], v[240:241]
	v_cvt_pk_fp8_f32 v247, v24, v25
	v_pk_fma_f32 v[26:27], v[26:27], v[238:239], v[242:243]
	s_nop 0
	v_cvt_pk_fp8_f32 v247, v26, v27 op_sel:[0,0,1]
	s_nop 1
	s_mov_b32 vcc_lo, 0x55555555
	s_mov_b32 vcc_hi, 0x55555555
	v_cndmask_b32_dpp v252, v245, v244, vcc quad_perm:[1,0,3,2] row_mask:0xf bank_mask:0xf
	v_cndmask_b32_dpp v253, v247, v246, vcc quad_perm:[1,0,3,2] row_mask:0xf bank_mask:0xf
	s_mov_b32 vcc_lo, 0xaaaaaaaa
	s_mov_b32 vcc_hi, 0xaaaaaaaa
	v_cndmask_b32_dpp v245, v244, v245, vcc quad_perm:[1,0,3,2] row_mask:0xf bank_mask:0xf
	v_cndmask_b32_dpp v247, v246, v247, vcc quad_perm:[1,0,3,2] row_mask:0xf bank_mask:0xf
	s_mov_b32 vcc_lo, 0x33333333
	s_mov_b32 vcc_hi, 0x33333333
	v_cndmask_b32_dpp v248, v253, v252, vcc quad_perm:[2,3,0,1] row_mask:0xf bank_mask:0xf
	v_cndmask_b32_dpp v249, v247, v245, vcc quad_perm:[2,3,0,1] row_mask:0xf bank_mask:0xf
	s_mov_b32 vcc_lo, 0xcccccccc
	s_mov_b32 vcc_hi, 0xcccccccc
	v_cndmask_b32_dpp v250, v252, v253, vcc quad_perm:[2,3,0,1] row_mask:0xf bank_mask:0xf
	v_cndmask_b32_dpp v251, v245, v247, vcc quad_perm:[2,3,0,1] row_mask:0xf bank_mask:0xf
	global_store_dwordx4 v[6:7], v[248:251], off offset:-1024
	s_and_saveexec_b64 s[12:13], s[8:9]
	s_cbranch_execz .LBB0_708
	s_add_i32 s70, s37, -8
	s_add_u32 s68, s92, s14
	v_mul_f32_e32 v24, 0x3a000000, v145
	s_addc_u32 s69, s93, s15
	v_mov_b32_e32 v25, v34
	v_mov_b32_e32 v26, s70
	ds_write_b64 v26, v[24:25]
	global_store_dwordx2 v137, v[24:25], s[68:69]
.LBB0_708:
	s_or_b64 exec, exec, s[12:13]
	s_waitcnt vmcnt(17)
	v_lshlrev_b32_e32 v58, 16, v22
	v_and_b32_e32 v59, 0xffff0000, v22
	v_lshlrev_b32_e32 v56, 16, v23
	v_and_b32_e32 v57, 0xffff0000, v23
	v_add_f32_e32 v22, v58, v59
	v_add_f32_e32 v23, v56, v57
	s_waitcnt vmcnt(16)
	v_lshlrev_b32_e32 v52, 16, v20
	v_and_b32_e32 v53, 0xffff0000, v20
	v_lshlrev_b32_e32 v54, 16, v21
	v_and_b32_e32 v55, 0xffff0000, v21
	v_add_f32_e32 v22, v22, v23
	v_add_f32_e32 v20, v52, v53
	v_add_f32_e32 v21, v54, v55
	s_waitcnt vmcnt(15)
	v_lshlrev_b32_e32 v32, 16, v18
	v_and_b32_e32 v33, 0xffff0000, v18
	v_lshlrev_b32_e32 v30, 16, v19
	v_and_b32_e32 v31, 0xffff0000, v19
	v_add_f32_e32 v22, 0, v22
	v_add_f32_e32 v20, v20, v21
	v_add_f32_e32 v18, v32, v33
	v_add_f32_e32 v19, v30, v31
	v_add_f32_e32 v20, v22, v20
	v_add_f32_e32 v18, v18, v19
	s_waitcnt vmcnt(14)
	v_lshlrev_b32_e32 v26, 16, v16
	v_and_b32_e32 v27, 0xffff0000, v16
	v_lshlrev_b32_e32 v28, 16, v17
	v_and_b32_e32 v29, 0xffff0000, v17
	v_add_f32_e32 v18, v20, v18
	v_add_f32_e32 v16, v26, v27
	v_add_f32_e32 v17, v28, v29
	s_waitcnt vmcnt(13)
	v_lshlrev_b32_e32 v22, 16, v14
	v_and_b32_e32 v23, 0xffff0000, v14
	v_lshlrev_b32_e32 v20, 16, v15
	v_and_b32_e32 v21, 0xffff0000, v15
	v_add_f32_e32 v16, v16, v17
	v_add_f32_e32 v14, v22, v23
	v_add_f32_e32 v15, v20, v21
	v_add_f32_e32 v16, v18, v16
	v_add_f32_e32 v14, v14, v15
	v_add_f32_e32 v14, v16, v14
	s_waitcnt vmcnt(12)
	v_lshlrev_b32_e32 v16, 16, v12
	v_and_b32_e32 v17, 0xffff0000, v12
	v_lshlrev_b32_e32 v18, 16, v13
	v_and_b32_e32 v19, 0xffff0000, v13
	v_add_f32_e32 v12, v16, v17
	v_add_f32_e32 v13, v18, v19
	v_add_f32_e32 v12, v12, v13
	v_add_f32_e32 v24, v14, v12
	s_waitcnt vmcnt(11)
	v_lshlrev_b32_e32 v14, 16, v10
	v_and_b32_e32 v15, 0xffff0000, v10
	v_lshlrev_b32_e32 v12, 16, v11
	v_and_b32_e32 v13, 0xffff0000, v11
	v_add_f32_e32 v10, v14, v15
	v_add_f32_e32 v11, v12, v13
	v_add_f32_e32 v10, v10, v11
	v_add_f32_e32 v24, v24, v10
	s_waitcnt vmcnt(10)
	v_lshlrev_b32_e32 v10, 16, v8
	v_and_b32_e32 v11, 0xffff0000, v8
	v_lshlrev_b32_e32 v8, 16, v9
	v_and_b32_e32 v9, 0xffff0000, v9
	v_add_f32_e32 v25, v10, v11
	v_add_f32_e32 v34, v8, v9
	v_add_f32_e32 v25, v25, v34
	v_add_f32_e32 v24, v24, v25
	s_nop 1
	v_add_f32_dpp v24, v24, v24 quad_perm:[1,0,3,2] row_mask:0xf bank_mask:0xf bound_ctrl:1
	s_nop 1
	v_add_f32_dpp v24, v24, v24 quad_perm:[2,3,0,1] row_mask:0xf bank_mask:0xf bound_ctrl:1
	s_nop 1
	v_add_f32_dpp v24, v24, v24 row_half_mirror row_mask:0xf bank_mask:0xf bound_ctrl:1
	s_nop 1
	v_add_f32_dpp v24, v24, v24 row_mirror row_mask:0xf bank_mask:0xf bound_ctrl:1
	v_mov_b32_e32 v25, v24
	s_nop 1
	v_permlane16_swap_b32_e32 v24, v25
	v_add_f32_e32 v24, v24, v25
	v_mov_b32_e32 v25, v24
	s_nop 1
	v_permlane32_swap_b32_e32 v24, v25
	v_add_f32_e32 v25, v24, v25
	v_fmac_f32_e32 v57, 0xba000000, v25
	v_fmac_f32_e32 v59, 0xba000000, v25
	v_fmac_f32_e32 v56, 0xba000000, v25
	v_fmac_f32_e32 v58, 0xba000000, v25
	v_mul_f32_e32 v24, v59, v59
	v_mul_f32_e32 v34, v57, v57
	v_fmac_f32_e32 v24, v58, v58
	v_fmac_f32_e32 v34, v56, v56
	v_fmac_f32_e32 v55, 0xba000000, v25
	v_fmac_f32_e32 v53, 0xba000000, v25
	v_add_f32_e32 v24, v24, v34
	v_fmac_f32_e32 v54, 0xba000000, v25
	v_fmac_f32_e32 v52, 0xba000000, v25
	v_mul_f32_e32 v34, v53, v53
	v_mul_f32_e32 v60, v55, v55
	v_fmac_f32_e32 v34, v52, v52
	v_fmac_f32_e32 v60, v54, v54
	v_add_f32_e32 v34, v34, v60
	v_fmac_f32_e32 v31, 0xba000000, v25
	v_fmac_f32_e32 v33, 0xba000000, v25
	v_add_f32_e32 v24, v24, v34
	v_fmac_f32_e32 v30, 0xba000000, v25
	v_fmac_f32_e32 v32, 0xba000000, v25
	v_mul_f32_e32 v34, v33, v33
	v_mul_f32_e32 v60, v31, v31
	v_fmac_f32_e32 v34, v32, v32
	v_fmac_f32_e32 v60, v30, v30
	v_add_f32_e32 v34, v34, v60
	v_fmac_f32_e32 v29, 0xba000000, v25
	v_fmac_f32_e32 v27, 0xba000000, v25
	v_add_f32_e32 v24, v34, v24
	v_fmac_f32_e32 v28, 0xba000000, v25
	v_fmac_f32_e32 v26, 0xba000000, v25
	v_mul_f32_e32 v34, v27, v27
	v_mul_f32_e32 v60, v29, v29
	v_fmac_f32_e32 v34, v26, v26
	v_fmac_f32_e32 v60, v28, v28
	v_add_f32_e32 v34, v34, v60
	v_fmac_f32_e32 v21, 0xba000000, v25
	v_fmac_f32_e32 v23, 0xba000000, v25
	v_add_f32_e32 v24, v34, v24
	v_fmac_f32_e32 v20, 0xba000000, v25
	v_fmac_f32_e32 v22, 0xba000000, v25
	v_mul_f32_e32 v34, v23, v23
	v_mul_f32_e32 v60, v21, v21
	v_fmac_f32_e32 v34, v22, v22
	v_fmac_f32_e32 v60, v20, v20
	v_add_f32_e32 v34, v34, v60
	v_fmac_f32_e32 v19, 0xba000000, v25
	v_fmac_f32_e32 v17, 0xba000000, v25
	v_add_f32_e32 v24, v34, v24
	v_fmac_f32_e32 v18, 0xba000000, v25
	v_fmac_f32_e32 v16, 0xba000000, v25
	v_mul_f32_e32 v34, v17, v17
	v_mul_f32_e32 v60, v19, v19
	v_fmac_f32_e32 v34, v16, v16
	v_fmac_f32_e32 v60, v18, v18
	v_add_f32_e32 v34, v34, v60
	v_fmac_f32_e32 v13, 0xba000000, v25
	v_fmac_f32_e32 v15, 0xba000000, v25
	v_add_f32_e32 v24, v34, v24
	v_fmac_f32_e32 v12, 0xba000000, v25
	v_fmac_f32_e32 v14, 0xba000000, v25
	v_mul_f32_e32 v34, v15, v15
	v_mul_f32_e32 v60, v13, v13
	v_fmac_f32_e32 v34, v14, v14
	v_fmac_f32_e32 v60, v12, v12
	v_add_f32_e32 v34, v34, v60
	v_fmac_f32_e32 v9, 0xba000000, v25
	v_fmac_f32_e32 v11, 0xba000000, v25
	v_add_f32_e32 v24, v34, v24
	v_fmac_f32_e32 v8, 0xba000000, v25
	v_fmac_f32_e32 v10, 0xba000000, v25
	v_mul_f32_e32 v34, v11, v11
	v_mul_f32_e32 v60, v9, v9
	v_fmac_f32_e32 v34, v10, v10
	v_fmac_f32_e32 v60, v8, v8
	v_add_f32_e32 v34, v34, v60
	v_add_f32_e32 v24, v34, v24
	s_nop 1
	v_add_f32_dpp v24, v24, v24 quad_perm:[1,0,3,2] row_mask:0xf bank_mask:0xf bound_ctrl:1
	s_nop 1
	v_add_f32_dpp v24, v24, v24 quad_perm:[2,3,0,1] row_mask:0xf bank_mask:0xf bound_ctrl:1
	s_nop 1
	v_add_f32_dpp v24, v24, v24 row_half_mirror row_mask:0xf bank_mask:0xf bound_ctrl:1
	s_nop 1
	v_add_f32_dpp v24, v24, v24 row_mirror row_mask:0xf bank_mask:0xf bound_ctrl:1
	v_mov_b32_e32 v34, v24
	s_nop 1
	v_permlane16_swap_b32_e32 v24, v34
	v_add_f32_e32 v24, v24, v34
	v_mov_b32_e32 v34, v24
	s_nop 1
	v_permlane32_swap_b32_e32 v24, v34
	v_add_f32_e32 v24, v24, v34
	v_fmamk_f32 v24, v24, 0x3a000000, v135
	v_cmp_gt_f32_e32 vcc, s44, v24
	v_mul_f32_e32 v34, 0x4f800000, v24
	s_nop 0
	v_cndmask_b32_e32 v24, v24, v34, vcc
	v_sqrt_f32_e32 v34, v24
	s_nop 0
	v_add_u32_e32 v60, -1, v34
	v_fma_f32 v61, -v60, v34, v24
	v_cmp_ge_f32_e64 s[12:13], 0, v61
	v_add_u32_e32 v61, 1, v34
	s_nop 0
	v_cndmask_b32_e64 v60, v34, v60, s[12:13]
	v_fma_f32 v34, -v61, v34, v24
	v_cmp_lt_f32_e64 s[12:13], 0, v34
	s_nop 1
	v_cndmask_b32_e64 v34, v60, v61, s[12:13]
	v_mul_f32_e32 v60, 0x37800000, v34
	v_cndmask_b32_e32 v34, v34, v60, vcc
	v_cmp_class_f32_e32 vcc, v24, v136
	s_nop 1
	v_cndmask_b32_e32 v24, v34, v24, vcc
	v_div_scale_f32 v34, s[12:13], v24, v24, 1.0
	v_rcp_f32_e32 v60, v34
	s_nop 0
	v_fma_f32 v61, -v34, v60, 1.0
	v_fmac_f32_e32 v60, v61, v60
	v_div_scale_f32 v61, vcc, 1.0, v24, 1.0
	v_mul_f32_e32 v62, v61, v60
	v_fma_f32 v63, -v34, v62, v61
	v_fmac_f32_e32 v62, v63, v60
	v_fma_f32 v34, -v34, v62, v61
	v_div_fmas_f32 v34, v34, v60, v62
	v_div_fixup_f32 v24, v34, v24, 1.0
	v_pk_mul_f32 v[58:59], v[58:59], v[24:25] op_sel_hi:[1,0]
	v_pk_mul_f32 v[56:57], v[56:57], v[24:25] op_sel_hi:[1,0]
	v_pk_fma_f32 v[58:59], v[180:181], v[58:59], v[184:185]
	v_pk_fma_f32 v[56:57], v[182:183], v[56:57], v[186:187]
	v_cvt_pk_fp8_f32 v244, v58, v59
	v_pk_mul_f32 v[52:53], v[52:53], v[24:25] op_sel_hi:[1,0]
	v_pk_mul_f32 v[54:55], v[54:55], v[24:25] op_sel_hi:[1,0]
	v_pk_mul_f32 v[32:33], v[32:33], v[24:25] op_sel_hi:[1,0]
	v_cvt_pk_fp8_f32 v244, v56, v57 op_sel:[0,0,1]
	v_pk_mul_f32 v[30:31], v[30:31], v[24:25] op_sel_hi:[1,0]
	v_pk_mul_f32 v[26:27], v[26:27], v[24:25] op_sel_hi:[1,0]
	v_pk_mul_f32 v[28:29], v[28:29], v[24:25] op_sel_hi:[1,0]
	v_pk_mul_f32 v[22:23], v[22:23], v[24:25] op_sel_hi:[1,0]
	v_pk_mul_f32 v[20:21], v[20:21], v[24:25] op_sel_hi:[1,0]
	v_pk_mul_f32 v[16:17], v[16:17], v[24:25] op_sel_hi:[1,0]
	v_pk_fma_f32 v[52:53], v[188:189], v[52:53], v[192:193]
	v_pk_fma_f32 v[54:55], v[190:191], v[54:55], v[194:195]
	v_cvt_pk_fp8_f32 v245, v52, v53
	v_pk_mul_f32 v[18:19], v[18:19], v[24:25] op_sel_hi:[1,0]
	v_pk_mul_f32 v[14:15], v[14:15], v[24:25] op_sel_hi:[1,0]
	v_pk_mul_f32 v[12:13], v[12:13], v[24:25] op_sel_hi:[1,0]
	v_cvt_pk_fp8_f32 v245, v54, v55 op_sel:[0,0,1]
	v_pk_mul_f32 v[10:11], v[10:11], v[24:25] op_sel_hi:[1,0]
	v_pk_mul_f32 v[8:9], v[8:9], v[24:25] op_sel_hi:[1,0]
	v_pk_fma_f32 v[32:33], v[32:33], v[196:197], v[200:201]
	s_nop 0
	v_cvt_pk_fp8_f32 v246, v32, v33
	v_pk_fma_f32 v[30:31], v[30:31], v[198:199], v[202:203]
	s_nop 0
	v_cvt_pk_fp8_f32 v246, v30, v31 op_sel:[0,0,1]
	v_pk_fma_f32 v[26:27], v[26:27], v[204:205], v[208:209]
	v_cvt_pk_fp8_f32 v247, v26, v27
	v_pk_fma_f32 v[28:29], v[28:29], v[206:207], v[210:211]
	s_nop 0
	v_cvt_pk_fp8_f32 v247, v28, v29 op_sel:[0,0,1]
	s_nop 1
	s_mov_b32 vcc_lo, 0x55555555
	s_mov_b32 vcc_hi, 0x55555555
	v_cndmask_b32_dpp v252, v245, v244, vcc quad_perm:[1,0,3,2] row_mask:0xf bank_mask:0xf
	v_cndmask_b32_dpp v253, v247, v246, vcc quad_perm:[1,0,3,2] row_mask:0xf bank_mask:0xf
	s_mov_b32 vcc_lo, 0xaaaaaaaa
	s_mov_b32 vcc_hi, 0xaaaaaaaa
	v_cndmask_b32_dpp v245, v244, v245, vcc quad_perm:[1,0,3,2] row_mask:0xf bank_mask:0xf
	v_cndmask_b32_dpp v247, v246, v247, vcc quad_perm:[1,0,3,2] row_mask:0xf bank_mask:0xf
	s_mov_b32 vcc_lo, 0x33333333
	s_mov_b32 vcc_hi, 0x33333333
	v_cndmask_b32_dpp v248, v253, v252, vcc quad_perm:[2,3,0,1] row_mask:0xf bank_mask:0xf
	v_cndmask_b32_dpp v249, v247, v245, vcc quad_perm:[2,3,0,1] row_mask:0xf bank_mask:0xf
	s_mov_b32 vcc_lo, 0xcccccccc
	s_mov_b32 vcc_hi, 0xcccccccc
	v_cndmask_b32_dpp v250, v252, v253, vcc quad_perm:[2,3,0,1] row_mask:0xf bank_mask:0xf
	v_cndmask_b32_dpp v251, v245, v247, vcc quad_perm:[2,3,0,1] row_mask:0xf bank_mask:0xf
	global_store_dwordx4 v[6:7], v[248:251], off
	v_pk_fma_f32 v[22:23], v[22:23], v[212:213], v[216:217]
	v_cvt_pk_fp8_f32 v244, v22, v23
	v_pk_fma_f32 v[20:21], v[20:21], v[214:215], v[218:219]
	s_nop 0
	v_cvt_pk_fp8_f32 v244, v20, v21 op_sel:[0,0,1]
	v_pk_fma_f32 v[16:17], v[16:17], v[220:221], v[224:225]
	v_cvt_pk_fp8_f32 v245, v16, v17
	v_pk_fma_f32 v[18:19], v[18:19], v[222:223], v[226:227]
	s_nop 0
	v_cvt_pk_fp8_f32 v245, v18, v19 op_sel:[0,0,1]
	v_pk_fma_f32 v[14:15], v[14:15], v[228:229], v[232:233]
	v_cvt_pk_fp8_f32 v246, v14, v15
	v_pk_fma_f32 v[12:13], v[12:13], v[230:231], v[234:235]
	s_nop 0
	v_cvt_pk_fp8_f32 v246, v12, v13 op_sel:[0,0,1]
	v_pk_fma_f32 v[10:11], v[10:11], v[236:237], v[240:241]
	v_cvt_pk_fp8_f32 v247, v10, v11
	v_pk_fma_f32 v[8:9], v[8:9], v[238:239], v[242:243]
	s_nop 0
	v_cvt_pk_fp8_f32 v247, v8, v9 op_sel:[0,0,1]
	s_nop 1
	s_mov_b32 vcc_lo, 0x55555555
	s_mov_b32 vcc_hi, 0x55555555
	v_cndmask_b32_dpp v252, v245, v244, vcc quad_perm:[1,0,3,2] row_mask:0xf bank_mask:0xf
	v_cndmask_b32_dpp v253, v247, v246, vcc quad_perm:[1,0,3,2] row_mask:0xf bank_mask:0xf
	s_mov_b32 vcc_lo, 0xaaaaaaaa
	s_mov_b32 vcc_hi, 0xaaaaaaaa
	v_cndmask_b32_dpp v245, v244, v245, vcc quad_perm:[1,0,3,2] row_mask:0xf bank_mask:0xf
	v_cndmask_b32_dpp v247, v246, v247, vcc quad_perm:[1,0,3,2] row_mask:0xf bank_mask:0xf
	s_mov_b32 vcc_lo, 0x33333333
	s_mov_b32 vcc_hi, 0x33333333
	v_cndmask_b32_dpp v248, v253, v252, vcc quad_perm:[2,3,0,1] row_mask:0xf bank_mask:0xf
	v_cndmask_b32_dpp v249, v247, v245, vcc quad_perm:[2,3,0,1] row_mask:0xf bank_mask:0xf
	s_mov_b32 vcc_lo, 0xcccccccc
	s_mov_b32 vcc_hi, 0xcccccccc
	v_cndmask_b32_dpp v250, v252, v253, vcc quad_perm:[2,3,0,1] row_mask:0xf bank_mask:0xf
	v_cndmask_b32_dpp v251, v245, v247, vcc quad_perm:[2,3,0,1] row_mask:0xf bank_mask:0xf
	global_store_dwordx4 v[6:7], v[248:251], off offset:1024
	s_and_saveexec_b64 s[12:13], s[8:9]
	s_cbranch_execz .LBB0_705
	s_add_u32 s68, s92, s14
	v_mul_f32_e32 v6, 0x3a000000, v25
	s_addc_u32 s69, s93, s15
	v_mov_b32_e32 v7, v24
	v_mov_b32_e32 v8, s37
	ds_write_b64 v8, v[6:7]
	global_store_dwordx2 v137, v[6:7], s[68:69] offset:8
	s_branch .LBB0_705
